# baseline (speedup 1.0000x reference)
.LBB2_70:
	s_and_b64 vcc, exec, s[30:31]
	s_cbranch_vccz .LBB2_112
	v_cmp_gt_u32_e64 s[0:1], 10, v0
	s_mov_b32 s25, 0
	s_nop 0
	v_cndmask_b32_e64 v2, 0, v0, s[0:1]
	v_mad_u64_u32 v[2:3], s[2:3], s24, 10, v[2:3]
	v_mov_b32_e32 v3, 0
	s_waitcnt lgkmcnt(0)
	v_lshl_add_u64 v[4:5], v[2:3], 2, s[14:15]
	global_load_dword v6, v[4:5], off
	s_lshl_b64 s[2:3], s[24:25], 2
	s_add_u32 s2, s16, s2
	s_addc_u32 s3, s17, s3
	s_load_dword s14, s[2:3], 0x0
	s_mul_i32 s2, s24, 0x30000
	s_add_u32 s2, s18, s2
	s_addc_u32 s3, s19, 0
	v_lshlrev_b32_e32 v4, 2, v0
	v_add_u32_e32 v2, 0x2000, v4
	global_load_dword v20, v2, s[2:3] offset:-4096 nt
	global_load_dword v22, v2, s[2:3] nt
	v_add_u32_e32 v2, 0x4000, v4
	global_load_dword v18, v2, s[2:3] offset:-4096 nt
	global_load_dword v24, v2, s[2:3] nt
	v_add_u32_e32 v2, 0x6000, v4
	global_load_dword v21, v2, s[2:3] offset:-4096 nt
	global_load_dword v23, v2, s[2:3] nt
	v_add_u32_e32 v2, 0x8000, v4
	global_load_dword v19, v2, s[2:3] offset:-4096 nt
	global_load_dword v25, v2, s[2:3] nt
	v_add_u32_e32 v2, 0xa000, v4
	global_load_dword v29, v2, s[2:3] offset:-4096 nt
	v_add_u32_e32 v2, 0xc000, v4
	global_load_dword v5, v2, s[2:3] offset:-4096 nt
	global_load_dword v26, v2, s[2:3] nt
	v_add_u32_e32 v2, 0xe000, v4
	global_load_dword v31, v2, s[2:3] offset:-4096 nt
	global_load_dword v30, v2, s[2:3] nt
	v_add_u32_e32 v2, 0x10000, v4
	global_load_dword v34, v2, s[2:3] offset:-4096 nt
	global_load_dword v28, v2, s[2:3] nt
	v_add_u32_e32 v2, 0x12000, v4
	global_load_dword v35, v2, s[2:3] offset:-4096 nt
	global_load_dword v42, v2, s[2:3] nt
	v_add_u32_e32 v2, 0x14000, v4
	global_load_dword v46, v2, s[2:3] offset:-4096 nt
	global_load_dword v39, v2, s[2:3] nt
	v_add_u32_e32 v2, 0x16000, v4
	global_load_dword v45, v2, s[2:3] offset:-4096 nt
	v_add_u32_e32 v2, 0x18000, v4
	global_load_dword v27, v2, s[2:3] nt
	v_add_u32_e32 v2, 0x1a000, v4
	global_load_dword v33, v2, s[2:3] offset:-4096 nt
	global_load_dword v32, v2, s[2:3] nt
	v_add_u32_e32 v2, 0x1c000, v4
	global_load_dword v36, v2, s[2:3] offset:-4096 nt
	global_load_dword v47, v4, s[2:3] nt
	global_load_dword v37, v2, s[2:3] nt
	v_add_u32_e32 v2, 0x1e000, v4
	global_load_dword v41, v2, s[2:3] offset:-4096 nt
	global_load_dword v40, v2, s[2:3] nt
	v_add_u32_e32 v2, 0x20000, v4
	global_load_dword v44, v2, s[2:3] offset:-4096 nt
	global_load_dword v38, v2, s[2:3] nt
	v_add_u32_e32 v2, 0x22000, v4
	global_load_dword v43, v2, s[2:3] offset:-4096 nt
	s_waitcnt lgkmcnt(0)
	s_add_i32 s15, s14, 0x7f
	s_and_b32 s15, s15, 0xffffff80
	v_cmp_gt_i32_e32 vcc, s15, v0
	s_nop 1
	s_mov_b64 s[46:47], vcc
	s_and_saveexec_b64 s[6:7], vcc
	s_cbranch_execz .LBB2_85
	s_cmpk_gt_i32 s14, 0x360
	s_cselect_b64 s[8:9], -1, 0
	s_cmpk_lt_i32 s14, 0x361
	s_cbranch_scc1 .LBB2_74
	v_add_u32_e32 v2, 0x24000, v4
	global_load_dword v7, v2, s[2:3]
	v_add_u32_e32 v2, 0x26000, v4
	global_load_dword v8, v2, s[2:3] offset:-4096
	global_load_dword v9, v2, s[2:3]
	v_add_u32_e32 v2, 0x28000, v4
	global_load_dword v10, v2, s[2:3] offset:-4096
	global_load_dword v11, v2, s[2:3]
	v_add_u32_e32 v2, 0x2a000, v4
	global_load_dword v12, v2, s[2:3] offset:-4096
	global_load_dword v13, v2, s[2:3]
	v_add_u32_e32 v2, 0x2c000, v4
	global_load_dword v14, v2, s[2:3] offset:-4096
	global_load_dword v15, v2, s[2:3]
	v_add_u32_e32 v2, 0x2e000, v4
	global_load_dword v16, v2, s[2:3] offset:-4096

.LBB2_85:
	s_or_b64 exec, exec, s[6:7]
	s_andn2_b64 exec, exec, s[46:47]
	s_cbranch_execz .Lz_skip
	s_waitcnt vmcnt(0)
	v_mov_b32_e32 v3, 0
	v_mov_b32_e32 v25, 0
	v_mov_b32_e32 v24, 0
	v_mov_b32_e32 v23, 0
	v_mov_b32_e32 v22, 0
	v_mov_b32_e32 v21, 0
	v_mov_b32_e32 v20, 0
	v_mov_b32_e32 v19, 0
	v_mov_b32_e32 v18, 0
	v_mov_b32_e32 v2, 0
.Lz_skip:
	s_or_b64 exec, exec, s[46:47]
	v_mov_b32_e32 v1, 0x7140
	v_mad_u32_u24 v1, v17, 48, v1
	v_add_f32_dpp v3, v3, v3 quad_perm:[1,0,3,2] row_mask:0xf bank_mask:0xf bound_ctrl:1
	v_add_f32_dpp v25, v25, v25 quad_perm:[1,0,3,2] row_mask:0xf bank_mask:0xf bound_ctrl:1
	v_add_f32_dpp v24, v24, v24 quad_perm:[1,0,3,2] row_mask:0xf bank_mask:0xf bound_ctrl:1
	v_add_f32_dpp v23, v23, v23 quad_perm:[1,0,3,2] row_mask:0xf bank_mask:0xf bound_ctrl:1
	v_add_f32_dpp v22, v22, v22 quad_perm:[1,0,3,2] row_mask:0xf bank_mask:0xf bound_ctrl:1
	v_add_f32_dpp v21, v21, v21 quad_perm:[1,0,3,2] row_mask:0xf bank_mask:0xf bound_ctrl:1
	v_add_f32_dpp v20, v20, v20 quad_perm:[1,0,3,2] row_mask:0xf bank_mask:0xf bound_ctrl:1
	v_add_f32_dpp v19, v19, v19 quad_perm:[1,0,3,2] row_mask:0xf bank_mask:0xf bound_ctrl:1
	v_add_f32_dpp v18, v18, v18 quad_perm:[1,0,3,2] row_mask:0xf bank_mask:0xf bound_ctrl:1
	v_add_f32_dpp v2, v2, v2 quad_perm:[1,0,3,2] row_mask:0xf bank_mask:0xf bound_ctrl:1
	v_add_f32_dpp v3, v3, v3 quad_perm:[2,3,0,1] row_mask:0xf bank_mask:0xf bound_ctrl:1
	v_add_f32_dpp v25, v25, v25 quad_perm:[2,3,0,1] row_mask:0xf bank_mask:0xf bound_ctrl:1
	v_add_f32_dpp v24, v24, v24 quad_perm:[2,3,0,1] row_mask:0xf bank_mask:0xf bound_ctrl:1
	v_add_f32_dpp v23, v23, v23 quad_perm:[2,3,0,1] row_mask:0xf bank_mask:0xf bound_ctrl:1
	v_add_f32_dpp v22, v22, v22 quad_perm:[2,3,0,1] row_mask:0xf bank_mask:0xf bound_ctrl:1
	v_add_f32_dpp v21, v21, v21 quad_perm:[2,3,0,1] row_mask:0xf bank_mask:0xf bound_ctrl:1
	v_add_f32_dpp v20, v20, v20 quad_perm:[2,3,0,1] row_mask:0xf bank_mask:0xf bound_ctrl:1
	v_add_f32_dpp v19, v19, v19 quad_perm:[2,3,0,1] row_mask:0xf bank_mask:0xf bound_ctrl:1
	v_add_f32_dpp v18, v18, v18 quad_perm:[2,3,0,1] row_mask:0xf bank_mask:0xf bound_ctrl:1
	v_add_f32_dpp v2, v2, v2 quad_perm:[2,3,0,1] row_mask:0xf bank_mask:0xf bound_ctrl:1
	v_add_f32_dpp v3, v3, v3 row_half_mirror row_mask:0xf bank_mask:0xf bound_ctrl:1
	v_add_f32_dpp v25, v25, v25 row_half_mirror row_mask:0xf bank_mask:0xf bound_ctrl:1
	v_add_f32_dpp v24, v24, v24 row_half_mirror row_mask:0xf bank_mask:0xf bound_ctrl:1
	v_add_f32_dpp v23, v23, v23 row_half_mirror row_mask:0xf bank_mask:0xf bound_ctrl:1
	v_add_f32_dpp v22, v22, v22 row_half_mirror row_mask:0xf bank_mask:0xf bound_ctrl:1
	v_add_f32_dpp v21, v21, v21 row_half_mirror row_mask:0xf bank_mask:0xf bound_ctrl:1
	v_add_f32_dpp v20, v20, v20 row_half_mirror row_mask:0xf bank_mask:0xf bound_ctrl:1
	v_add_f32_dpp v19, v19, v19 row_half_mirror row_mask:0xf bank_mask:0xf bound_ctrl:1
	v_add_f32_dpp v18, v18, v18 row_half_mirror row_mask:0xf bank_mask:0xf bound_ctrl:1
	v_add_f32_dpp v2, v2, v2 row_half_mirror row_mask:0xf bank_mask:0xf bound_ctrl:1
	v_add_f32_dpp v3, v3, v3 row_mirror row_mask:0xf bank_mask:0xf bound_ctrl:1
	v_add_f32_dpp v25, v25, v25 row_mirror row_mask:0xf bank_mask:0xf bound_ctrl:1
	v_add_f32_dpp v24, v24, v24 row_mirror row_mask:0xf bank_mask:0xf bound_ctrl:1
	v_add_f32_dpp v23, v23, v23 row_mirror row_mask:0xf bank_mask:0xf bound_ctrl:1
	v_add_f32_dpp v22, v22, v22 row_mirror row_mask:0xf bank_mask:0xf bound_ctrl:1
	v_add_f32_dpp v21, v21, v21 row_mirror row_mask:0xf bank_mask:0xf bound_ctrl:1
	v_add_f32_dpp v20, v20, v20 row_mirror row_mask:0xf bank_mask:0xf bound_ctrl:1
	v_add_f32_dpp v19, v19, v19 row_mirror row_mask:0xf bank_mask:0xf bound_ctrl:1
	v_add_f32_dpp v18, v18, v18 row_mirror row_mask:0xf bank_mask:0xf bound_ctrl:1
	v_add_f32_dpp v2, v2, v2 row_mirror row_mask:0xf bank_mask:0xf bound_ctrl:1
	v_add_f32_dpp v3, v3, v3 row_bcast:15 row_mask:0xa bank_mask:0xf
	v_add_f32_dpp v25, v25, v25 row_bcast:15 row_mask:0xa bank_mask:0xf
	v_add_f32_dpp v24, v24, v24 row_bcast:15 row_mask:0xa bank_mask:0xf
	v_add_f32_dpp v23, v23, v23 row_bcast:15 row_mask:0xa bank_mask:0xf
	v_add_f32_dpp v22, v22, v22 row_bcast:15 row_mask:0xa bank_mask:0xf
	v_add_f32_dpp v21, v21, v21 row_bcast:15 row_mask:0xa bank_mask:0xf
	v_add_f32_dpp v20, v20, v20 row_bcast:15 row_mask:0xa bank_mask:0xf
	v_add_f32_dpp v19, v19, v19 row_bcast:15 row_mask:0xa bank_mask:0xf
	v_add_f32_dpp v18, v18, v18 row_bcast:15 row_mask:0xa bank_mask:0xf
	v_add_f32_dpp v2, v2, v2 row_bcast:15 row_mask:0xa bank_mask:0xf
	v_add_f32_dpp v3, v3, v3 row_bcast:31 row_mask:0xc bank_mask:0xf
	v_add_f32_dpp v25, v25, v25 row_bcast:31 row_mask:0xc bank_mask:0xf
	v_add_f32_dpp v24, v24, v24 row_bcast:31 row_mask:0xc bank_mask:0xf
	v_add_f32_dpp v23, v23, v23 row_bcast:31 row_mask:0xc bank_mask:0xf
	v_add_f32_dpp v22, v22, v22 row_bcast:31 row_mask:0xc bank_mask:0xf
	v_add_f32_dpp v21, v21, v21 row_bcast:31 row_mask:0xc bank_mask:0xf
	v_add_f32_dpp v20, v20, v20 row_bcast:31 row_mask:0xc bank_mask:0xf
	v_add_f32_dpp v19, v19, v19 row_bcast:31 row_mask:0xc bank_mask:0xf
	v_add_f32_dpp v18, v18, v18 row_bcast:31 row_mask:0xc bank_mask:0xf
	v_add_f32_dpp v2, v2, v2 row_bcast:31 row_mask:0xc bank_mask:0xf
	s_mov_b64 s[2:3], exec
	s_mov_b32 exec_lo, 0
	s_brev_b32 exec_hi, 1
	ds_write2_b32 v1, v3, v25 offset0:0 offset1:1
	ds_write2_b32 v1, v24, v23 offset0:2 offset1:3
	ds_write2_b32 v1, v22, v21 offset0:4 offset1:5
	ds_write2_b32 v1, v20, v19 offset0:6 offset1:7
	ds_write2_b32 v1, v18, v2 offset0:8 offset1:9
	s_mov_b64 exec, s[2:3]
	s_or_b64 exec, exec, s[2:3]
	v_cmp_gt_u32_e32 vcc, 64, v0
	s_waitcnt lgkmcnt(0)
	s_barrier
	s_and_saveexec_b64 s[2:3], vcc
	s_cbranch_execz .LBB2_111
	v_mov_b32_e32 v1, 0
	s_and_saveexec_b64 s[6:7], s[0:1]
	s_cbranch_execz .LBB2_108
	v_lshlrev_b32_e32 v1, 2, v0
	s_waitcnt vmcnt(1)
	v_add_u32_e32 v7, 0x7000, v1
	ds_read2_b32 v[2:3], v7 offset0:80 offset1:92
	ds_read2_b32 v[4:5], v7 offset0:104 offset1:116
	ds_read2_b32 v[8:9], v7 offset0:128 offset1:140
	ds_read2_b32 v[10:11], v7 offset0:152 offset1:164
	ds_read2_b32 v[12:13], v7 offset0:176 offset1:188
	s_waitcnt lgkmcnt(4)
	v_add_f32_e32 v2, 0, v2
	v_add_f32_e32 v2, v2, v3
	s_waitcnt lgkmcnt(3)
	v_add_f32_e32 v2, v2, v4
	v_add_f32_e32 v2, v2, v5
	s_waitcnt lgkmcnt(2)
	v_add_f32_e32 v2, v2, v8
	v_add_f32_e32 v2, v2, v9
	s_waitcnt lgkmcnt(1)
	v_add_f32_e32 v4, v2, v10
	ds_read2_b32 v[2:3], v7 offset0:200 offset1:212
	v_add_f32_e32 v4, v4, v11
	s_waitcnt lgkmcnt(1)
	v_add_f32_e32 v4, v4, v12
	v_add_f32_e32 v8, v4, v13
	ds_read2_b32 v[4:5], v7 offset0:224 offset1:236
	v_add_u32_e32 v1, 0x7200, v1
	s_waitcnt lgkmcnt(1)
	v_add_f32_e32 v2, v8, v2
	ds_read2_b32 v[8:9], v1 offset0:120 offset1:132
	v_add_f32_e32 v1, v2, v3
	s_waitcnt lgkmcnt(1)
	v_add_f32_e32 v1, v1, v4
	v_cvt_f32_i32_e32 v2, s14
	v_add_f32_e32 v1, v1, v5
	s_waitcnt lgkmcnt(0)
	v_add_f32_e32 v1, v1, v8
	v_add_f32_e32 v1, v1, v9
	v_div_scale_f32 v3, s[0:1], v2, v2, v1
	v_rcp_f32_e32 v4, v3
	s_mov_b32 s8, 0x42c80000
	v_fma_f32 v5, -v3, v4, 1.0
	v_fmac_f32_e32 v4, v5, v4
	v_div_scale_f32 v5, vcc, v1, v2, v1
	v_mul_f32_e32 v7, v5, v4
	v_fma_f32 v8, -v3, v7, v5
	v_fmac_f32_e32 v7, v8, v4
	v_fma_f32 v3, -v3, v7, v5
	v_div_fmas_f32 v3, v3, v4, v7
	v_div_fixup_f32 v1, v3, v2, v1
	s_waitcnt vmcnt(0)
	v_sub_f32_e32 v1, v1, v6
	v_mul_f32_e32 v2, 0.5, v1
	v_mul_f32_e32 v1, v1, v2
	v_div_scale_f32 v2, s[0:1], s8, s8, v1
	v_rcp_f32_e32 v3, v2
	s_nop 0
	v_fma_f32 v4, -v2, v3, 1.0
	v_fmac_f32_e32 v3, v4, v3
	v_div_scale_f32 v4, vcc, v1, s8, v1
	v_mul_f32_e32 v5, v4, v3
	v_fma_f32 v6, -v2, v5, v4
	v_fmac_f32_e32 v5, v6, v3
	v_fma_f32 v2, -v2, v5, v4
	v_div_fmas_f32 v2, v2, v3, v5
	v_div_fixup_f32 v1, v2, s8, v1
